# scan swizzle + second conversion item issued on even steps and finished at the end of the next (odd) step, so its memory time spans two steps
# baseline (speedup 1.0000x reference)
.LBB0_422:
	s_ashr_i32 s11, s51, 16
	s_bfe_u32 s92, s51, 0x5000b
	v_readlane_b32 s76, v254, 36
	s_cmp_eq_u32 s11, 1
	v_readlane_b32 s77, v254, 37
	v_readlane_b32 s78, v254, 38
	v_readlane_b32 s79, v254, 39
	v_readlane_b32 s80, v254, 40
	v_readlane_b32 s81, v254, 41
	v_readlane_b32 s82, v254, 42
	v_readlane_b32 s83, v254, 43
	s_cselect_b32 s0, s76, s78
	s_cselect_b32 s1, s77, s79
	v_readlane_b32 s68, v254, 44
	s_cmp_lt_u32 s51, 0x10000
	v_readlane_b32 s82, v254, 58
	v_readlane_b32 s83, v254, 59
	s_cselect_b32 s1, s83, s1
	s_cselect_b32 s0, s82, s0
	s_lshl_b32 s12, s92, 24
	s_add_u32 s28, s0, s12
	s_addc_u32 s29, s1, 0
	v_readlane_b32 s69, v254, 45
	v_readlane_b32 s70, v254, 46
	v_readlane_b32 s71, v254, 47
	v_readlane_b32 s72, v254, 48
	v_readlane_b32 s73, v254, 49
	v_readlane_b32 s74, v254, 50
	v_readlane_b32 s75, v254, 51
	s_cmp_eq_u32 s92, 0
	s_cselect_b64 s[90:91], -1, 0
	v_readlane_b32 s60, v254, 20
	v_readlane_b32 s78, v254, 54
	v_readlane_b32 s79, v254, 55
	s_and_b64 s[0:1], s[90:91], exec
	v_readlane_b32 s74, v254, 34
	v_readlane_b32 s75, v254, 35
	s_cselect_b32 s30, s74, s78
	s_cselect_b32 s31, s75, s79
	s_cmp_eq_u32 s11, 3
	s_cselect_b64 s[52:53], -1, 0
	s_and_b64 s[0:1], s[52:53], exec
	s_cselect_b32 s1, s31, s29
	s_cselect_b32 s0, s30, s28
	s_and_b32 s43, s46, 0x7e0
	s_and_b32 s98, s51, 0x7c0
	s_lshl_b32 s98, s98, 13
	s_lshl_b32 s40, s43, 2
	s_add_u32 s98, s98, s40
	s_add_u32 s100, s0, s98
	s_addc_u32 s101, s1, 0
	global_load_dwordx4 v[152:155], v250, s[100:101]
	v_add_u32_e32 v253, 0x2000, v250
	global_load_dwordx4 v[156:159], v253, s[100:101]
	v_add_u32_e32 v252, 0x4000, v250
	global_load_dwordx4 v[160:163], v252, s[100:101]
	v_add_u32_e32 v253, 0x6000, v250
	global_load_dwordx4 v[164:167], v253, s[100:101]
	v_add_u32_e32 v252, 0x8000, v250
	global_load_dwordx4 v[168:171], v252, s[100:101]
	v_add_u32_e32 v253, 0xa000, v250
	global_load_dwordx4 v[172:175], v253, s[100:101]
	v_add_u32_e32 v252, 0xc000, v250
	global_load_dwordx4 v[176:179], v252, s[100:101]
	v_add_u32_e32 v253, 0xe000, v250
	global_load_dwordx4 v[246:249], v253, s[100:101]
	s_lshr_b32 s98, s49, 9
	s_lshl_b32 s98, s98, 8
	s_cmp_lt_u32 s7, 60
	s_cselect_b32 s0, s98, 0
	s_cselect_b32 s1, s7, 0
	s_and_b32 s1, s1, 1
	s_cmp_lg_u32 s1, 0
	s_cselect_b64 s[94:95], -1, 0
	s_add_i32 s0, s0, s44
	s_lshl_b32 s0, s0, 3
	v_readlane_b32 s1, v255, 15
	s_add_i32 s28, s1, s0
	s_bfe_u32 s93, s28, 0x5000b
	s_ashr_i32 s57, s28, 16
	s_lshl_b32 s13, s93, 22
	s_cmp_eq_u32 s57, 3
	s_cselect_b64 s[96:97], -1, 0
	s_cmp_eq_u32 s93, 0
	s_cselect_b64 s[0:1], -1, 0
	s_lshl_b32 s34, s28, 5
	s_and_b32 s37, s34, 0x7e0
	s_and_b32 s36, s28, 0x7c0
	s_mov_b32 s38, s86
	s_and_b32 s98, s7, 1
	s_cmp_gt_u32 s7, 59
	s_cselect_b32 s98, 1, s98
	s_cmp_lg_u32 s98, 0
	v_readlane_b32 s76, v254, 52
	v_readlane_b32 s77, v254, 53
	v_readlane_b32 s80, v254, 56
	v_readlane_b32 s81, v254, 57
	v_readlane_b32 s61, v254, 21
	v_readlane_b32 s62, v254, 22
	v_readlane_b32 s63, v254, 23
	v_readlane_b32 s64, v254, 24
	v_readlane_b32 s65, v254, 25
	v_readlane_b32 s66, v254, 26
	v_readlane_b32 s67, v254, 27
	v_readlane_b32 s68, v254, 28
	v_readlane_b32 s69, v254, 29
	v_readlane_b32 s70, v254, 30
	v_readlane_b32 s71, v254, 31
	v_readlane_b32 s72, v254, 32
	v_readlane_b32 s73, v254, 33
	s_cbranch_scc1 .LBB0_424
	v_readlane_b32 s80, v254, 36
	s_cmp_eq_u32 s57, 1
	v_readlane_b32 s81, v254, 37
	v_readlane_b32 s82, v254, 38
	v_readlane_b32 s83, v254, 39
	s_cselect_b32 s29, s80, s82
	s_cselect_b32 s30, s81, s83
	v_readlane_b32 s68, v254, 44
	s_cmp_lt_u32 s28, 0x10000
	v_readlane_b32 s82, v254, 58
	v_readlane_b32 s83, v254, 59
	s_cselect_b32 s28, s83, s30
	s_cselect_b32 s29, s82, s29
	s_lshl_b32 s30, s13, 2
	v_readlane_b32 s69, v254, 45
	v_readlane_b32 s70, v254, 46
	v_readlane_b32 s71, v254, 47
	v_readlane_b32 s72, v254, 48
	v_readlane_b32 s73, v254, 49
	v_readlane_b32 s74, v254, 50
	v_readlane_b32 s75, v254, 51
	s_add_u32 s30, s29, s30
	s_addc_u32 s31, s28, 0
	v_readlane_b32 s60, v254, 20
	v_readlane_b32 s78, v254, 54
	v_readlane_b32 s79, v254, 55
	s_and_b64 s[28:29], s[0:1], exec
	v_readlane_b32 s74, v254, 34
	v_readlane_b32 s75, v254, 35
	s_cselect_b32 s60, s74, s78
	s_cselect_b32 vcc_lo, s75, s79
	s_and_b64 s[28:29], s[96:97], exec
	s_cselect_b32 s29, vcc_lo, s31
	s_cselect_b32 s28, s60, s30
	s_lshl_b32 s98, s36, 13
	s_lshl_b32 s40, s37, 2
	s_add_u32 s98, s98, s40
	s_add_u32 s100, s28, s98
	s_addc_u32 s101, s29, 0
	global_load_dwordx4 v[2:5], v250, s[100:101]
	v_add_u32_e32 v253, 0x2000, v250
	global_load_dwordx4 v[6:9], v253, s[100:101]
	v_add_u32_e32 v252, 0x4000, v250
	global_load_dwordx4 v[10:13], v252, s[100:101]
	v_add_u32_e32 v253, 0x6000, v250
	global_load_dwordx4 v[14:17], v253, s[100:101]
	v_add_u32_e32 v252, 0x8000, v250
	global_load_dwordx4 v[18:21], v252, s[100:101]
	v_add_u32_e32 v253, 0xa000, v250
	global_load_dwordx4 v[22:25], v253, s[100:101]
	v_add_u32_e32 v252, 0xc000, v250
	global_load_dwordx4 v[26:29], v252, s[100:101]
	v_add_u32_e32 v253, 0xe000, v250
	global_load_dwordx4 v[116:119], v253, s[100:101]
	v_readlane_b32 s84, v254, 40
	v_readlane_b32 s85, v254, 41
	v_readlane_b32 s86, v254, 42
	v_readlane_b32 s87, v254, 43
	v_readlane_b32 s76, v254, 52
	v_readlane_b32 s77, v254, 53
	v_readlane_b32 s80, v254, 56
	v_readlane_b32 s81, v254, 57
	v_readlane_b32 s61, v254, 21
	v_readlane_b32 s62, v254, 22
	v_readlane_b32 s63, v254, 23
	v_readlane_b32 s64, v254, 24
	v_readlane_b32 s65, v254, 25
	v_readlane_b32 s66, v254, 26
	v_readlane_b32 s67, v254, 27
	v_readlane_b32 s68, v254, 28
	v_readlane_b32 s69, v254, 29
	v_readlane_b32 s70, v254, 30
	v_readlane_b32 s71, v254, 31
	v_readlane_b32 s72, v254, 32
	v_readlane_b32 s73, v254, 33

.LBB0_455:
	s_lshl_b32 s7, s92, 22
	s_lshl_b32 s7, s7, 1
	s_add_u32 s7, s35, s7
	s_addc_u32 s28, s33, 0
	s_add_u32 s29, s56, s12
	s_addc_u32 s30, s39, 0
	s_cmp_eq_u32 s11, 2
	s_cselect_b32 s7, s7, s29
	s_cselect_b32 s30, s28, s30
	s_and_b64 s[28:29], s[90:91], exec
	s_mov_b32 s12, 0x2400000
	v_readlane_b32 s80, v254, 36
	s_cselect_b32 s28, s12, 0x4300000
	v_readlane_b32 s86, v254, 42
	v_readlane_b32 s87, v254, 43
	s_add_u32 s31, s86, s28
	s_addc_u32 s60, s87, 0
	s_and_b64 s[28:29], s[52:53], exec
	s_cselect_b32 s29, s60, s30
	s_cselect_b32 s28, s31, s7
	s_lshl_b32 s7, s43, 1
	s_and_b32 s30, s46, 0x60
	s_lshl_b32 s31, s11, 7
	s_and_b32 s7, s7, 0xf00
	s_or_b32 s30, s31, s30
	s_add_i32 s30, s30, s7
	s_cmp_gt_i32 s11, 1
	s_cselect_b32 s7, s43, s30
	s_ashr_i32 s11, s7, 3
	s_andn2_b32 s11, s11, 31
	s_or_b32 s30, s11, s50
	s_ashr_i32 s31, s30, 31
	s_lshl_b64 s[30:31], s[30:31], 8
	s_and_b32 s7, s7, 0xe0
	s_or_b32 s7, s30, s7
	s_mov_b32 s100, s7
	s_mov_b32 s101, s31
	s_lshl_b64 s[100:101], s[100:101], 7
	s_add_u32 s100, s100, s28
	s_addc_u32 s101, s101, s29
	s_and_b32 s98, s47, 64
	s_cmp_gt_u32 s47, 0xeff
	s_cselect_b32 s98, 1, s98
	s_cmp_lg_u32 s98, 0
	s_cbranch_scc1 .Lcvw_all
	s_waitcnt vmcnt(9)
	s_branch .Lcvw_done
.Lcvw_all:
	s_waitcnt vmcnt(1)
.Lcvw_done:
	v_cvt_pk_bf16_f32 v152, v152, v156
	v_cvt_pk_bf16_f32 v156, v153, v157
	v_cvt_pk_bf16_f32 v238, v154, v158
	v_cvt_pk_bf16_f32 v242, v155, v159
	v_cvt_pk_bf16_f32 v153, v160, v164
	v_cvt_pk_bf16_f32 v157, v161, v165
	v_cvt_pk_bf16_f32 v239, v162, v166
	v_cvt_pk_bf16_f32 v243, v163, v167
	v_cvt_pk_bf16_f32 v154, v168, v172
	v_cvt_pk_bf16_f32 v158, v169, v173
	v_cvt_pk_bf16_f32 v240, v170, v174
	v_cvt_pk_bf16_f32 v244, v171, v175
	v_cvt_pk_bf16_f32 v155, v176, v246
	v_cvt_pk_bf16_f32 v159, v177, v247
	v_cvt_pk_bf16_f32 v241, v178, v248
	v_cvt_pk_bf16_f32 v245, v179, v249
	global_store_dwordx4 v251, v[152:155], s[100:101]
	global_store_dwordx4 v251, v[156:159], s[100:101] offset:128
	global_store_dwordx4 v251, v[238:241], s[100:101] offset:256
	global_store_dwordx4 v251, v[242:245], s[100:101] offset:384
	s_andn2_b64 vcc, exec, s[94:95]
	s_mov_b32 s86, s38
	v_readlane_b32 s81, v254, 37
	v_readlane_b32 s82, v254, 38
	v_readlane_b32 s83, v254, 39
	v_readlane_b32 s84, v254, 40
	v_readlane_b32 s85, v254, 41
	s_cbranch_vccnz .LBB0_410
	s_lshl_b32 s7, s13, 1
	s_add_u32 s7, s35, s7
	s_addc_u32 s11, s33, 0
	s_lshl_b32 s28, s93, 24
	s_add_u32 s28, s56, s28
	s_addc_u32 s29, s39, 0
	s_cmp_eq_u32 s57, 2
	s_cselect_b32 s7, s7, s28
	s_cselect_b32 s11, s11, s29
	s_and_b64 s[0:1], s[0:1], exec
	s_mov_b32 s0, 0x2400000
	v_readlane_b32 s72, v254, 36
	s_cselect_b32 s0, s0, 0x4300000
	v_readlane_b32 s78, v254, 42
	v_readlane_b32 s79, v254, 43
	s_add_u32 s28, s78, s0
	s_addc_u32 s29, s79, 0
	s_and_b64 s[0:1], s[96:97], exec
	s_cselect_b32 s1, s29, s11
	s_cselect_b32 s0, s28, s7
	s_lshl_b32 s7, s37, 1
	s_and_b32 s11, s34, 0x60
	s_lshl_b32 s28, s57, 7
	s_and_b32 s7, s7, 0xf00
	s_or_b32 s11, s28, s11
	s_add_i32 s11, s11, s7
	s_cmp_gt_i32 s57, 1
	s_cselect_b32 s7, s37, s11
	s_ashr_i32 s11, s7, 3
	s_andn2_b32 s11, s11, 31
	s_lshr_b32 s28, s36, 6
	s_or_b32 s28, s11, s28
	s_ashr_i32 s29, s28, 31
	s_lshl_b64 s[28:29], s[28:29], 8
	s_and_b32 s7, s7, 0xe0
	s_or_b32 s7, s28, s7
	v_readlane_b32 s73, v254, 37
	v_readlane_b32 s74, v254, 38
	v_readlane_b32 s75, v254, 39
	v_readlane_b32 s76, v254, 40
	v_readlane_b32 s77, v254, 41
	s_mov_b32 s100, s7
	s_mov_b32 s101, s29
	s_lshl_b64 s[100:101], s[100:101], 7
	s_add_u32 s100, s100, s0
	s_addc_u32 s101, s101, s1
	v_cvt_pk_bf16_f32 v2, v2, v6
	v_cvt_pk_bf16_f32 v6, v3, v7
	v_cvt_pk_bf16_f32 v238, v4, v8
	v_cvt_pk_bf16_f32 v242, v5, v9
	v_cvt_pk_bf16_f32 v3, v10, v14
	v_cvt_pk_bf16_f32 v7, v11, v15
	v_cvt_pk_bf16_f32 v239, v12, v16
	v_cvt_pk_bf16_f32 v243, v13, v17
	v_cvt_pk_bf16_f32 v4, v18, v22
	v_cvt_pk_bf16_f32 v8, v19, v23
	v_cvt_pk_bf16_f32 v240, v20, v24
	v_cvt_pk_bf16_f32 v244, v21, v25
	v_cvt_pk_bf16_f32 v5, v26, v116
	v_cvt_pk_bf16_f32 v9, v27, v117
	v_cvt_pk_bf16_f32 v241, v28, v118
	v_cvt_pk_bf16_f32 v245, v29, v119
	global_store_dwordx4 v251, v[2:5], s[100:101]
	global_store_dwordx4 v251, v[6:9], s[100:101] offset:128
	global_store_dwordx4 v251, v[238:241], s[100:101] offset:256
	global_store_dwordx4 v251, v[242:245], s[100:101] offset:384
	s_branch .LBB0_410
